# baseline (speedup 1.0000x reference)
_Z5k_csrPKjS0_PKfPjPfPDF16_P15HIP_vector_typeIjLj4EE:
	s_load_dwordx2 s[4:5], s[0:1], 0x0
	s_load_dwordx2 s[6:7], s[0:1], 0x10
	s_mul_i32 s3, s2, 0xc4
	v_lshrrev_b32_e32 v25, 4, v0
	v_add_u32_e32 v28, s3, v25
	v_and_b32_e32 v1, 15, v0
	v_min_i32_e32 v4, 0xc34f, v28
	v_add_u32_e32 v26, 64, v28
	v_lshlrev_b32_e32 v18, 4, v1
	v_mov_b32_e32 v19, 0
	v_ashrrev_i32_e32 v5, 31, v4
	v_min_i32_e32 v6, 0xc34f, v26
	s_waitcnt lgkmcnt(0)
	v_lshl_add_u64 v[2:3], s[6:7], 0, v[18:19]
	v_lshlrev_b64 v[4:5], 8, v[4:5]
	v_ashrrev_i32_e32 v7, 31, v6
	v_lshl_add_u64 v[4:5], v[2:3], 0, v[4:5]
	v_lshlrev_b64 v[6:7], 8, v[6:7]
	v_add_u32_e32 v24, 0x80, v28
	v_lshl_add_u64 v[6:7], v[2:3], 0, v[6:7]
	global_load_dwordx4 v[14:17], v[4:5], off nt
	global_load_dwordx4 v[10:13], v[6:7], off nt
	v_min_i32_e32 v4, 0xc34f, v24
	v_or_b32_e32 v32, 0xc00, v0
	v_ashrrev_i32_e32 v5, 31, v4
	v_lshrrev_b32_e32 v23, 4, v32
	v_lshlrev_b64 v[4:5], 8, v[4:5]
	v_add_u32_e32 v22, s3, v23
	v_lshl_add_u64 v[20:21], v[2:3], 0, v[4:5]
	v_min_i32_e32 v4, 0xc34f, v22
	v_ashrrev_i32_e32 v5, 31, v4
	v_lshlrev_b64 v[4:5], 8, v[4:5]
	v_lshrrev_b32_e32 v1, 3, v0
	v_lshl_add_u64 v[30:31], v[2:3], 0, v[4:5]
	global_load_dwordx4 v[6:9], v[20:21], off nt
	global_load_dwordx4 v[2:5], v[30:31], off nt
	v_min_u32_e32 v20, 0x7c, v1
	s_mul_i32 s6, s2, 0x7d
	v_add_u32_e32 v30, s6, v20
	v_ashrrev_i32_e32 v31, 31, v30
	v_lshl_add_u64 v[30:31], v[30:31], 2, s[4:5]
	global_load_dword v21, v[30:31], off nt
	global_load_dword v27, v[30:31], off offset:500 nt
	v_cmp_gt_u32_e32 vcc, 2, v0
	v_lshlrev_b32_e32 v1, 2, v0
	s_and_saveexec_b64 s[4:5], vcc
	v_lshlrev_b32_e32 v18, 2, v0
	ds_write_b32 v18, v19 offset:22528
	s_or_b64 exec, exec, s[4:5]
	s_movk_i32 s4, 0x100
	v_cmp_gt_u32_e64 s[8:9], s4, v0
	s_and_saveexec_b64 s[4:5], s[8:9]
	s_cbranch_execz .LBB1_4
	s_mov_b32 s6, 0x539782a
	v_mul_hi_u32 v29, v0, s6
	s_movk_i32 s6, 0xffcf
	v_lshlrev_b32_e32 v18, 2, v0
	v_mov_b32_e32 v19, 0
	v_mad_i32_i24 v29, v29, s6, v0
	ds_write2st64_b32 v18, v19, v29 offset0:64 offset1:72

_Z7k_headsPKfS0_S0_S0_S0_Pf:
	s_load_dwordx8 s[4:11], s[0:1], 0x8
	s_load_dwordx2 s[12:13], s[0:1], 0x0
	s_load_dwordx2 s[14:15], s[0:1], 0x28
	v_lshrrev_b32_e32 v36, 2, v0
	s_movk_i32 s2, 0x100
	v_lshlrev_b32_e32 v34, 9, v36
	v_mov_b32_e32 v35, 0
	s_waitcnt lgkmcnt(0)
	v_lshl_add_u64 v[2:3], s[4:5], 0, v[34:35]
	v_mov_b32_e32 v1, s9
	v_cmp_gt_u32_e32 vcc, s2, v0
	v_and_b32_e32 v37, 3, v0
	v_lshlrev_b32_e32 v34, 7, v37
	v_cndmask_b32_e32 v3, v1, v3, vcc
	v_mov_b32_e32 v1, s8
	v_cndmask_b32_e32 v2, v1, v2, vcc
	v_lshl_add_u64 v[38:39], v[2:3], 0, v[34:35]
	global_load_dwordx4 v[18:21], v[38:39], off offset:48
	global_load_dwordx4 v[22:25], v[38:39], off offset:32
	global_load_dwordx4 v[26:29], v[38:39], off offset:16
	global_load_dwordx4 v[30:33], v[38:39], off
	global_load_dwordx4 v[2:5], v[38:39], off offset:112
	global_load_dwordx4 v[6:9], v[38:39], off offset:96
	global_load_dwordx4 v[10:13], v[38:39], off offset:80
	global_load_dwordx4 v[14:17], v[38:39], off offset:64
	v_min_u32_e32 v1, 63, v36
	v_lshlrev_b32_e32 v38, 2, v1
	v_mov_b32_e32 v39, v35
	v_lshl_add_u64 v[38:39], s[6:7], 0, v[38:39]
	v_mov_b32_e32 v1, s11
	v_cndmask_b32_e32 v39, v1, v39, vcc
	v_mov_b32_e32 v1, s10
	v_cndmask_b32_e32 v38, v1, v38, vcc
	global_load_dword v38, v[38:39], off
	s_movk_i32 s2, 0x80
	v_cmp_gt_u32_e32 vcc, s2, v0
	s_and_saveexec_b64 s[2:3], vcc
	s_cbranch_execz .LBB4_2
	v_mov_b32_e32 v1, v35
	v_lshl_add_u64 v[40:41], v[0:1], 2, s[12:13]
	global_load_dword v1, v[40:41], off nt
	global_load_dword v35, v[40:41], off offset:512 nt
	global_load_dword v39, v[40:41], off offset:1024 nt
	global_load_dword v42, v[40:41], off offset:1536 nt
	global_load_dword v43, v[40:41], off offset:2048 nt
	global_load_dword v44, v[40:41], off offset:2560 nt
	global_load_dword v45, v[40:41], off offset:3072 nt
	global_load_dword v46, v[40:41], off offset:3584 nt
	s_movk_i32 s4, 0x1000
	v_add_co_u32_e32 v40, vcc, s4, v40
	s_waitcnt vmcnt(7)
	v_add_f32_e32 v1, 0, v1
	v_addc_co_u32_e32 v41, vcc, 0, v41, vcc
	global_load_dword v47, v[40:41], off nt
	global_load_dword v48, v[40:41], off offset:512 nt
	global_load_dword v49, v[40:41], off offset:1024 nt
	global_load_dword v50, v[40:41], off offset:1536 nt
	global_load_dword v51, v[40:41], off offset:2048 nt
	global_load_dword v52, v[40:41], off offset:2560 nt
	global_load_dword v53, v[40:41], off offset:3072 nt
	global_load_dword v54, v[40:41], off offset:3584 nt
	s_waitcnt vmcnt(14)
	v_add_f32_e32 v1, v1, v35
	s_waitcnt vmcnt(13)
	v_add_f32_e32 v1, v1, v39
	s_waitcnt vmcnt(12)
	v_add_f32_e32 v1, v1, v42
	s_waitcnt vmcnt(11)
	v_add_f32_e32 v1, v1, v43
	s_waitcnt vmcnt(10)
	v_add_f32_e32 v1, v1, v44
	s_waitcnt vmcnt(9)
	v_add_f32_e32 v1, v1, v45
	s_waitcnt vmcnt(8)
	v_add_f32_e32 v1, v1, v46
	v_lshlrev_b32_e32 v35, 2, v0
	s_waitcnt vmcnt(7)
	v_add_f32_e32 v1, v1, v47
	s_waitcnt vmcnt(6)
	v_add_f32_e32 v1, v1, v48
	s_waitcnt vmcnt(5)
	v_add_f32_e32 v1, v1, v49
	s_waitcnt vmcnt(4)
	v_add_f32_e32 v1, v1, v50
	s_waitcnt vmcnt(3)
	v_add_f32_e32 v1, v1, v51
	s_waitcnt vmcnt(2)
	v_add_f32_e32 v1, v1, v52
	s_waitcnt vmcnt(1)
	v_add_f32_e32 v1, v1, v53
	s_waitcnt vmcnt(0)
	v_add_f32_e32 v1, v1, v54
	v_mul_f32_e32 v1, 0x37a7c5ac, v1
	ds_write_b32 v35, v1
